# v68 + expert gate/up epilogue (silu*up -> fp8) rewritten with packed f32 multiplies/adds (same f32 math, fewer VALU ops)
# speedup vs baseline: 1.0102x; 1.0043x over previous
.LBB0_5248:
	s_or_b64 exec, exec, s[34:35]
	s_lshl_b32 s0, s30, 7
	v_lshl_add_u32 v6, s61, 8, v5
	s_and_b32 s0, s0, 0x380
	v_lshlrev_b32_e32 v2, 3, v2
	v_ashrrev_i32_e32 v3, 31, v2
	s_or_b32 s92, s0, s55
	v_lshl_add_u64 v[2:3], v[2:3], 0, s[92:93]
	v_lshl_add_u64 v[2:3], s[14:15], 0, v[2:3]
	s_mov_b32 s98, 0xbfb8aa3b
	v_mul_f32_e32 v28, 0x41800000, v20
	v_pk_mul_f32 v[190:191], v[190:191], v[20:21] op_sel_hi:[1,0]
	v_pk_mul_f32 v[192:193], v[192:193], v[20:21] op_sel_hi:[1,0]
	v_pk_mul_f32 v[186:187], v[186:187], v[28:29] op_sel_hi:[1,0]
	v_pk_mul_f32 v[188:189], v[188:189], v[28:29] op_sel_hi:[1,0]
	v_pk_mul_f32 v[22:23], v[190:191], s[98:99] op_sel_hi:[1,0]
	v_pk_mul_f32 v[24:25], v[192:193], s[98:99] op_sel_hi:[1,0]
	v_exp_f32_e32 v22, v22
	v_exp_f32_e32 v23, v23
	v_exp_f32_e32 v24, v24
	v_exp_f32_e32 v25, v25
	v_pk_mul_f32 v[190:191], v[190:191], v[186:187]
	v_pk_add_f32 v[22:23], v[22:23], 1.0 op_sel_hi:[1,0]
	v_pk_add_f32 v[24:25], v[24:25], 1.0 op_sel_hi:[1,0]
	v_rcp_f32_e32 v22, v22
	v_rcp_f32_e32 v23, v23
	v_rcp_f32_e32 v24, v24
	v_rcp_f32_e32 v25, v25
	v_pk_mul_f32 v[192:193], v[192:193], v[188:189]
	v_pk_mul_f32 v[190:191], v[190:191], v[22:23]
	v_pk_mul_f32 v[192:193], v[192:193], v[24:25]
	v_med3_f32 v190, v190, s76, v237
	v_med3_f32 v191, v191, s76, v237
	v_med3_f32 v192, v192, s76, v237
	v_med3_f32 v193, v193, s76, v237
	v_cvt_pk_fp8_f32 v26, v190, v191
	v_cvt_pk_fp8_f32 v26, v192, v193 op_sel:[0,0,1]
	v_pk_mul_f32 v[182:183], v[182:183], v[20:21] op_sel_hi:[1,0]
	v_pk_mul_f32 v[184:185], v[184:185], v[20:21] op_sel_hi:[1,0]
	v_pk_mul_f32 v[178:179], v[178:179], v[28:29] op_sel_hi:[1,0]
	v_pk_mul_f32 v[180:181], v[180:181], v[28:29] op_sel_hi:[1,0]
	v_pk_mul_f32 v[22:23], v[182:183], s[98:99] op_sel_hi:[1,0]
	v_pk_mul_f32 v[24:25], v[184:185], s[98:99] op_sel_hi:[1,0]
	v_exp_f32_e32 v22, v22
	v_exp_f32_e32 v23, v23
	v_exp_f32_e32 v24, v24
	v_exp_f32_e32 v25, v25
	v_pk_mul_f32 v[182:183], v[182:183], v[178:179]
	v_pk_add_f32 v[22:23], v[22:23], 1.0 op_sel_hi:[1,0]
	v_pk_add_f32 v[24:25], v[24:25], 1.0 op_sel_hi:[1,0]
	v_rcp_f32_e32 v22, v22
	v_rcp_f32_e32 v23, v23
	v_rcp_f32_e32 v24, v24
	v_rcp_f32_e32 v25, v25
	v_pk_mul_f32 v[184:185], v[184:185], v[180:181]
	v_pk_mul_f32 v[182:183], v[182:183], v[22:23]
	v_pk_mul_f32 v[184:185], v[184:185], v[24:25]
	v_med3_f32 v182, v182, s76, v237
	v_med3_f32 v183, v183, s76, v237
	v_med3_f32 v184, v184, s76, v237
	v_med3_f32 v185, v185, s76, v237
	v_cvt_pk_fp8_f32 v27, v182, v183
	v_cvt_pk_fp8_f32 v27, v184, v185 op_sel:[0,0,1]
	v_mov_b32_e32 v30, v6
	v_ashrrev_i32_e32 v31, 31, v30
	v_lshlrev_b64 v[30:31], 10, v[30:31]
	v_lshl_add_u64 v[30:31], v[30:31], 0, v[2:3]
	global_store_dwordx2 v[30:31], v[26:27], off
	v_mul_f32_e32 v28, 0x41800000, v18
	v_pk_mul_f32 v[174:175], v[174:175], v[18:19] op_sel_hi:[1,0]
	v_pk_mul_f32 v[176:177], v[176:177], v[18:19] op_sel_hi:[1,0]
	v_pk_mul_f32 v[170:171], v[170:171], v[28:29] op_sel_hi:[1,0]
	v_pk_mul_f32 v[172:173], v[172:173], v[28:29] op_sel_hi:[1,0]
	v_pk_mul_f32 v[22:23], v[174:175], s[98:99] op_sel_hi:[1,0]
	v_pk_mul_f32 v[24:25], v[176:177], s[98:99] op_sel_hi:[1,0]
	v_exp_f32_e32 v22, v22
	v_exp_f32_e32 v23, v23
	v_exp_f32_e32 v24, v24
	v_exp_f32_e32 v25, v25
	v_pk_mul_f32 v[174:175], v[174:175], v[170:171]
	v_pk_add_f32 v[22:23], v[22:23], 1.0 op_sel_hi:[1,0]
	v_pk_add_f32 v[24:25], v[24:25], 1.0 op_sel_hi:[1,0]
	v_rcp_f32_e32 v22, v22
	v_rcp_f32_e32 v23, v23
	v_rcp_f32_e32 v24, v24
	v_rcp_f32_e32 v25, v25
	v_pk_mul_f32 v[176:177], v[176:177], v[172:173]
	v_pk_mul_f32 v[174:175], v[174:175], v[22:23]
	v_pk_mul_f32 v[176:177], v[176:177], v[24:25]
	v_med3_f32 v174, v174, s76, v237
	v_med3_f32 v175, v175, s76, v237
	v_med3_f32 v176, v176, s76, v237
	v_med3_f32 v177, v177, s76, v237
	v_cvt_pk_fp8_f32 v26, v174, v175
	v_cvt_pk_fp8_f32 v26, v176, v177 op_sel:[0,0,1]
	v_pk_mul_f32 v[166:167], v[166:167], v[18:19] op_sel_hi:[1,0]
	v_pk_mul_f32 v[168:169], v[168:169], v[18:19] op_sel_hi:[1,0]
	v_pk_mul_f32 v[162:163], v[162:163], v[28:29] op_sel_hi:[1,0]
	v_pk_mul_f32 v[164:165], v[164:165], v[28:29] op_sel_hi:[1,0]
	v_pk_mul_f32 v[22:23], v[166:167], s[98:99] op_sel_hi:[1,0]
	v_pk_mul_f32 v[24:25], v[168:169], s[98:99] op_sel_hi:[1,0]
	v_exp_f32_e32 v22, v22
	v_exp_f32_e32 v23, v23
	v_exp_f32_e32 v24, v24
	v_exp_f32_e32 v25, v25
	v_pk_mul_f32 v[166:167], v[166:167], v[162:163]
	v_pk_add_f32 v[22:23], v[22:23], 1.0 op_sel_hi:[1,0]
	v_pk_add_f32 v[24:25], v[24:25], 1.0 op_sel_hi:[1,0]
	v_rcp_f32_e32 v22, v22
	v_rcp_f32_e32 v23, v23
	v_rcp_f32_e32 v24, v24
	v_rcp_f32_e32 v25, v25
	v_pk_mul_f32 v[168:169], v[168:169], v[164:165]
	v_pk_mul_f32 v[166:167], v[166:167], v[22:23]
	v_pk_mul_f32 v[168:169], v[168:169], v[24:25]
	v_med3_f32 v166, v166, s76, v237
	v_med3_f32 v167, v167, s76, v237
	v_med3_f32 v168, v168, s76, v237
	v_med3_f32 v169, v169, s76, v237
	v_cvt_pk_fp8_f32 v27, v166, v167
	v_cvt_pk_fp8_f32 v27, v168, v169 op_sel:[0,0,1]
	v_add_u32_e32 v30, 0x10, v6
	v_ashrrev_i32_e32 v31, 31, v30
	v_lshlrev_b64 v[30:31], 10, v[30:31]
	v_lshl_add_u64 v[30:31], v[30:31], 0, v[2:3]
	global_store_dwordx2 v[30:31], v[26:27], off
	v_mul_f32_e32 v28, 0x41800000, v16
	v_pk_mul_f32 v[158:159], v[158:159], v[16:17] op_sel_hi:[1,0]
	v_pk_mul_f32 v[160:161], v[160:161], v[16:17] op_sel_hi:[1,0]
	v_pk_mul_f32 v[154:155], v[154:155], v[28:29] op_sel_hi:[1,0]
	v_pk_mul_f32 v[156:157], v[156:157], v[28:29] op_sel_hi:[1,0]
	v_pk_mul_f32 v[22:23], v[158:159], s[98:99] op_sel_hi:[1,0]
	v_pk_mul_f32 v[24:25], v[160:161], s[98:99] op_sel_hi:[1,0]
	v_exp_f32_e32 v22, v22
	v_exp_f32_e32 v23, v23
	v_exp_f32_e32 v24, v24
	v_exp_f32_e32 v25, v25
	v_pk_mul_f32 v[158:159], v[158:159], v[154:155]
	v_pk_add_f32 v[22:23], v[22:23], 1.0 op_sel_hi:[1,0]
	v_pk_add_f32 v[24:25], v[24:25], 1.0 op_sel_hi:[1,0]
	v_rcp_f32_e32 v22, v22
	v_rcp_f32_e32 v23, v23
	v_rcp_f32_e32 v24, v24
	v_rcp_f32_e32 v25, v25
	v_pk_mul_f32 v[160:161], v[160:161], v[156:157]
	v_pk_mul_f32 v[158:159], v[158:159], v[22:23]
	v_pk_mul_f32 v[160:161], v[160:161], v[24:25]
	v_med3_f32 v158, v158, s76, v237
	v_med3_f32 v159, v159, s76, v237
	v_med3_f32 v160, v160, s76, v237
	v_med3_f32 v161, v161, s76, v237
	v_cvt_pk_fp8_f32 v26, v158, v159
	v_cvt_pk_fp8_f32 v26, v160, v161 op_sel:[0,0,1]
	v_pk_mul_f32 v[150:151], v[150:151], v[16:17] op_sel_hi:[1,0]
	v_pk_mul_f32 v[152:153], v[152:153], v[16:17] op_sel_hi:[1,0]
	v_pk_mul_f32 v[146:147], v[146:147], v[28:29] op_sel_hi:[1,0]
	v_pk_mul_f32 v[148:149], v[148:149], v[28:29] op_sel_hi:[1,0]
	v_pk_mul_f32 v[22:23], v[150:151], s[98:99] op_sel_hi:[1,0]
	v_pk_mul_f32 v[24:25], v[152:153], s[98:99] op_sel_hi:[1,0]
	v_exp_f32_e32 v22, v22
	v_exp_f32_e32 v23, v23
	v_exp_f32_e32 v24, v24
	v_exp_f32_e32 v25, v25
	v_pk_mul_f32 v[150:151], v[150:151], v[146:147]
	v_pk_add_f32 v[22:23], v[22:23], 1.0 op_sel_hi:[1,0]
	v_pk_add_f32 v[24:25], v[24:25], 1.0 op_sel_hi:[1,0]
	v_rcp_f32_e32 v22, v22
	v_rcp_f32_e32 v23, v23
	v_rcp_f32_e32 v24, v24
	v_rcp_f32_e32 v25, v25
	v_pk_mul_f32 v[152:153], v[152:153], v[148:149]
	v_pk_mul_f32 v[150:151], v[150:151], v[22:23]
	v_pk_mul_f32 v[152:153], v[152:153], v[24:25]
	v_med3_f32 v150, v150, s76, v237
	v_med3_f32 v151, v151, s76, v237
	v_med3_f32 v152, v152, s76, v237
	v_med3_f32 v153, v153, s76, v237
	v_cvt_pk_fp8_f32 v27, v150, v151
	v_cvt_pk_fp8_f32 v27, v152, v153 op_sel:[0,0,1]
	v_add_u32_e32 v30, 0x20, v6
	v_ashrrev_i32_e32 v31, 31, v30
	v_lshlrev_b64 v[30:31], 10, v[30:31]
	v_lshl_add_u64 v[30:31], v[30:31], 0, v[2:3]
	global_store_dwordx2 v[30:31], v[26:27], off
	v_mul_f32_e32 v28, 0x41800000, v14
	v_pk_mul_f32 v[142:143], v[142:143], v[14:15] op_sel_hi:[1,0]
	v_pk_mul_f32 v[144:145], v[144:145], v[14:15] op_sel_hi:[1,0]
	v_pk_mul_f32 v[138:139], v[138:139], v[28:29] op_sel_hi:[1,0]
	v_pk_mul_f32 v[140:141], v[140:141], v[28:29] op_sel_hi:[1,0]
	v_pk_mul_f32 v[22:23], v[142:143], s[98:99] op_sel_hi:[1,0]
	v_pk_mul_f32 v[24:25], v[144:145], s[98:99] op_sel_hi:[1,0]
	v_exp_f32_e32 v22, v22
	v_exp_f32_e32 v23, v23
	v_exp_f32_e32 v24, v24
	v_exp_f32_e32 v25, v25
	v_pk_mul_f32 v[142:143], v[142:143], v[138:139]
	v_pk_add_f32 v[22:23], v[22:23], 1.0 op_sel_hi:[1,0]
	v_pk_add_f32 v[24:25], v[24:25], 1.0 op_sel_hi:[1,0]
	v_rcp_f32_e32 v22, v22
	v_rcp_f32_e32 v23, v23
	v_rcp_f32_e32 v24, v24
	v_rcp_f32_e32 v25, v25
	v_pk_mul_f32 v[144:145], v[144:145], v[140:141]
	v_pk_mul_f32 v[142:143], v[142:143], v[22:23]
	v_pk_mul_f32 v[144:145], v[144:145], v[24:25]
	v_med3_f32 v142, v142, s76, v237
	v_med3_f32 v143, v143, s76, v237
	v_med3_f32 v144, v144, s76, v237
	v_med3_f32 v145, v145, s76, v237
	v_cvt_pk_fp8_f32 v26, v142, v143
	v_cvt_pk_fp8_f32 v26, v144, v145 op_sel:[0,0,1]
	v_pk_mul_f32 v[134:135], v[134:135], v[14:15] op_sel_hi:[1,0]
	v_pk_mul_f32 v[136:137], v[136:137], v[14:15] op_sel_hi:[1,0]
	v_pk_mul_f32 v[130:131], v[130:131], v[28:29] op_sel_hi:[1,0]
	v_pk_mul_f32 v[132:133], v[132:133], v[28:29] op_sel_hi:[1,0]
	v_pk_mul_f32 v[22:23], v[134:135], s[98:99] op_sel_hi:[1,0]
	v_pk_mul_f32 v[24:25], v[136:137], s[98:99] op_sel_hi:[1,0]
	v_exp_f32_e32 v22, v22
	v_exp_f32_e32 v23, v23
	v_exp_f32_e32 v24, v24
	v_exp_f32_e32 v25, v25
	v_pk_mul_f32 v[134:135], v[134:135], v[130:131]
	v_pk_add_f32 v[22:23], v[22:23], 1.0 op_sel_hi:[1,0]
	v_pk_add_f32 v[24:25], v[24:25], 1.0 op_sel_hi:[1,0]
	v_rcp_f32_e32 v22, v22
	v_rcp_f32_e32 v23, v23
	v_rcp_f32_e32 v24, v24
	v_rcp_f32_e32 v25, v25
	v_pk_mul_f32 v[136:137], v[136:137], v[132:133]
	v_pk_mul_f32 v[134:135], v[134:135], v[22:23]
	v_pk_mul_f32 v[136:137], v[136:137], v[24:25]
	v_med3_f32 v134, v134, s76, v237
	v_med3_f32 v135, v135, s76, v237
	v_med3_f32 v136, v136, s76, v237
	v_med3_f32 v137, v137, s76, v237
	v_cvt_pk_fp8_f32 v27, v134, v135
	v_cvt_pk_fp8_f32 v27, v136, v137 op_sel:[0,0,1]
	v_add_u32_e32 v30, 0x30, v6
	v_ashrrev_i32_e32 v31, 31, v30
	v_lshlrev_b64 v[30:31], 10, v[30:31]
	v_lshl_add_u64 v[30:31], v[30:31], 0, v[2:3]
	global_store_dwordx2 v[30:31], v[26:27], off
	v_mul_f32_e32 v28, 0x41800000, v12
	v_pk_mul_f32 v[126:127], v[126:127], v[12:13] op_sel_hi:[1,0]
	v_pk_mul_f32 v[128:129], v[128:129], v[12:13] op_sel_hi:[1,0]
	v_pk_mul_f32 v[122:123], v[122:123], v[28:29] op_sel_hi:[1,0]
	v_pk_mul_f32 v[124:125], v[124:125], v[28:29] op_sel_hi:[1,0]
	v_pk_mul_f32 v[22:23], v[126:127], s[98:99] op_sel_hi:[1,0]
	v_pk_mul_f32 v[24:25], v[128:129], s[98:99] op_sel_hi:[1,0]
	v_exp_f32_e32 v22, v22
	v_exp_f32_e32 v23, v23
	v_exp_f32_e32 v24, v24
	v_exp_f32_e32 v25, v25
	v_pk_mul_f32 v[126:127], v[126:127], v[122:123]
	v_pk_add_f32 v[22:23], v[22:23], 1.0 op_sel_hi:[1,0]
	v_pk_add_f32 v[24:25], v[24:25], 1.0 op_sel_hi:[1,0]
	v_rcp_f32_e32 v22, v22
	v_rcp_f32_e32 v23, v23
	v_rcp_f32_e32 v24, v24
	v_rcp_f32_e32 v25, v25
	v_pk_mul_f32 v[128:129], v[128:129], v[124:125]
	v_pk_mul_f32 v[126:127], v[126:127], v[22:23]
	v_pk_mul_f32 v[128:129], v[128:129], v[24:25]
	v_med3_f32 v126, v126, s76, v237
	v_med3_f32 v127, v127, s76, v237
	v_med3_f32 v128, v128, s76, v237
	v_med3_f32 v129, v129, s76, v237
	v_cvt_pk_fp8_f32 v26, v126, v127
	v_cvt_pk_fp8_f32 v26, v128, v129 op_sel:[0,0,1]
	v_pk_mul_f32 v[118:119], v[118:119], v[12:13] op_sel_hi:[1,0]
	v_pk_mul_f32 v[120:121], v[120:121], v[12:13] op_sel_hi:[1,0]
	v_pk_mul_f32 v[114:115], v[114:115], v[28:29] op_sel_hi:[1,0]
	v_pk_mul_f32 v[116:117], v[116:117], v[28:29] op_sel_hi:[1,0]
	v_pk_mul_f32 v[22:23], v[118:119], s[98:99] op_sel_hi:[1,0]
	v_pk_mul_f32 v[24:25], v[120:121], s[98:99] op_sel_hi:[1,0]
	v_exp_f32_e32 v22, v22
	v_exp_f32_e32 v23, v23
	v_exp_f32_e32 v24, v24
	v_exp_f32_e32 v25, v25
	v_pk_mul_f32 v[118:119], v[118:119], v[114:115]
	v_pk_add_f32 v[22:23], v[22:23], 1.0 op_sel_hi:[1,0]
	v_pk_add_f32 v[24:25], v[24:25], 1.0 op_sel_hi:[1,0]
	v_rcp_f32_e32 v22, v22
	v_rcp_f32_e32 v23, v23
	v_rcp_f32_e32 v24, v24
	v_rcp_f32_e32 v25, v25
	v_pk_mul_f32 v[120:121], v[120:121], v[116:117]
	v_pk_mul_f32 v[118:119], v[118:119], v[22:23]
	v_pk_mul_f32 v[120:121], v[120:121], v[24:25]
	v_med3_f32 v118, v118, s76, v237
	v_med3_f32 v119, v119, s76, v237
	v_med3_f32 v120, v120, s76, v237
	v_med3_f32 v121, v121, s76, v237
	v_cvt_pk_fp8_f32 v27, v118, v119
	v_cvt_pk_fp8_f32 v27, v120, v121 op_sel:[0,0,1]
	v_add_u32_e32 v30, 0x80, v6
	v_ashrrev_i32_e32 v31, 31, v30
	v_lshlrev_b64 v[30:31], 10, v[30:31]
	v_lshl_add_u64 v[30:31], v[30:31], 0, v[2:3]
	global_store_dwordx2 v[30:31], v[26:27], off
	v_mul_f32_e32 v28, 0x41800000, v10
	v_pk_mul_f32 v[110:111], v[110:111], v[10:11] op_sel_hi:[1,0]
	v_pk_mul_f32 v[112:113], v[112:113], v[10:11] op_sel_hi:[1,0]
	v_pk_mul_f32 v[106:107], v[106:107], v[28:29] op_sel_hi:[1,0]
	v_pk_mul_f32 v[108:109], v[108:109], v[28:29] op_sel_hi:[1,0]
	v_pk_mul_f32 v[22:23], v[110:111], s[98:99] op_sel_hi:[1,0]
	v_pk_mul_f32 v[24:25], v[112:113], s[98:99] op_sel_hi:[1,0]
	v_exp_f32_e32 v22, v22
	v_exp_f32_e32 v23, v23
	v_exp_f32_e32 v24, v24
	v_exp_f32_e32 v25, v25
	v_pk_mul_f32 v[110:111], v[110:111], v[106:107]
	v_pk_add_f32 v[22:23], v[22:23], 1.0 op_sel_hi:[1,0]
	v_pk_add_f32 v[24:25], v[24:25], 1.0 op_sel_hi:[1,0]
	v_rcp_f32_e32 v22, v22
	v_rcp_f32_e32 v23, v23
	v_rcp_f32_e32 v24, v24
	v_rcp_f32_e32 v25, v25
	v_pk_mul_f32 v[112:113], v[112:113], v[108:109]
	v_pk_mul_f32 v[110:111], v[110:111], v[22:23]
	v_pk_mul_f32 v[112:113], v[112:113], v[24:25]
	v_med3_f32 v110, v110, s76, v237
	v_med3_f32 v111, v111, s76, v237
	v_med3_f32 v112, v112, s76, v237
	v_med3_f32 v113, v113, s76, v237
	v_cvt_pk_fp8_f32 v26, v110, v111
	v_cvt_pk_fp8_f32 v26, v112, v113 op_sel:[0,0,1]
	v_pk_mul_f32 v[102:103], v[102:103], v[10:11] op_sel_hi:[1,0]
	v_pk_mul_f32 v[104:105], v[104:105], v[10:11] op_sel_hi:[1,0]
	v_pk_mul_f32 v[98:99], v[98:99], v[28:29] op_sel_hi:[1,0]
	v_pk_mul_f32 v[100:101], v[100:101], v[28:29] op_sel_hi:[1,0]
	v_pk_mul_f32 v[22:23], v[102:103], s[98:99] op_sel_hi:[1,0]
	v_pk_mul_f32 v[24:25], v[104:105], s[98:99] op_sel_hi:[1,0]
	v_exp_f32_e32 v22, v22
	v_exp_f32_e32 v23, v23
	v_exp_f32_e32 v24, v24
	v_exp_f32_e32 v25, v25
	v_pk_mul_f32 v[102:103], v[102:103], v[98:99]
	v_pk_add_f32 v[22:23], v[22:23], 1.0 op_sel_hi:[1,0]
	v_pk_add_f32 v[24:25], v[24:25], 1.0 op_sel_hi:[1,0]
	v_rcp_f32_e32 v22, v22
	v_rcp_f32_e32 v23, v23
	v_rcp_f32_e32 v24, v24
	v_rcp_f32_e32 v25, v25
	v_pk_mul_f32 v[104:105], v[104:105], v[100:101]
	v_pk_mul_f32 v[102:103], v[102:103], v[22:23]
	v_pk_mul_f32 v[104:105], v[104:105], v[24:25]
	v_med3_f32 v102, v102, s76, v237
	v_med3_f32 v103, v103, s76, v237
	v_med3_f32 v104, v104, s76, v237
	v_med3_f32 v105, v105, s76, v237
	v_cvt_pk_fp8_f32 v27, v102, v103
	v_cvt_pk_fp8_f32 v27, v104, v105 op_sel:[0,0,1]
	v_add_u32_e32 v30, 0x90, v6
	v_ashrrev_i32_e32 v31, 31, v30
	v_lshlrev_b64 v[30:31], 10, v[30:31]
	v_lshl_add_u64 v[30:31], v[30:31], 0, v[2:3]
	global_store_dwordx2 v[30:31], v[26:27], off
	v_mul_f32_e32 v28, 0x41800000, v8
	v_pk_mul_f32 v[94:95], v[94:95], v[8:9] op_sel_hi:[1,0]
	v_pk_mul_f32 v[96:97], v[96:97], v[8:9] op_sel_hi:[1,0]
	v_pk_mul_f32 v[90:91], v[90:91], v[28:29] op_sel_hi:[1,0]
	v_pk_mul_f32 v[92:93], v[92:93], v[28:29] op_sel_hi:[1,0]
	v_pk_mul_f32 v[22:23], v[94:95], s[98:99] op_sel_hi:[1,0]
	v_pk_mul_f32 v[24:25], v[96:97], s[98:99] op_sel_hi:[1,0]
	v_exp_f32_e32 v22, v22
	v_exp_f32_e32 v23, v23
	v_exp_f32_e32 v24, v24
	v_exp_f32_e32 v25, v25
	v_pk_mul_f32 v[94:95], v[94:95], v[90:91]
	v_pk_add_f32 v[22:23], v[22:23], 1.0 op_sel_hi:[1,0]
	v_pk_add_f32 v[24:25], v[24:25], 1.0 op_sel_hi:[1,0]
	v_rcp_f32_e32 v22, v22
	v_rcp_f32_e32 v23, v23
	v_rcp_f32_e32 v24, v24
	v_rcp_f32_e32 v25, v25
	v_pk_mul_f32 v[96:97], v[96:97], v[92:93]
	v_pk_mul_f32 v[94:95], v[94:95], v[22:23]
	v_pk_mul_f32 v[96:97], v[96:97], v[24:25]
	v_med3_f32 v94, v94, s76, v237
	v_med3_f32 v95, v95, s76, v237
	v_med3_f32 v96, v96, s76, v237
	v_med3_f32 v97, v97, s76, v237
	v_cvt_pk_fp8_f32 v26, v94, v95
	v_cvt_pk_fp8_f32 v26, v96, v97 op_sel:[0,0,1]
	v_pk_mul_f32 v[86:87], v[86:87], v[8:9] op_sel_hi:[1,0]
	v_pk_mul_f32 v[88:89], v[88:89], v[8:9] op_sel_hi:[1,0]
	v_pk_mul_f32 v[82:83], v[82:83], v[28:29] op_sel_hi:[1,0]
	v_pk_mul_f32 v[84:85], v[84:85], v[28:29] op_sel_hi:[1,0]
	v_pk_mul_f32 v[22:23], v[86:87], s[98:99] op_sel_hi:[1,0]
	v_pk_mul_f32 v[24:25], v[88:89], s[98:99] op_sel_hi:[1,0]
	v_exp_f32_e32 v22, v22
	v_exp_f32_e32 v23, v23
	v_exp_f32_e32 v24, v24
	v_exp_f32_e32 v25, v25
	v_pk_mul_f32 v[86:87], v[86:87], v[82:83]
	v_pk_add_f32 v[22:23], v[22:23], 1.0 op_sel_hi:[1,0]
	v_pk_add_f32 v[24:25], v[24:25], 1.0 op_sel_hi:[1,0]
	v_rcp_f32_e32 v22, v22
	v_rcp_f32_e32 v23, v23
	v_rcp_f32_e32 v24, v24
	v_rcp_f32_e32 v25, v25
	v_pk_mul_f32 v[88:89], v[88:89], v[84:85]
	v_pk_mul_f32 v[86:87], v[86:87], v[22:23]
	v_pk_mul_f32 v[88:89], v[88:89], v[24:25]
	v_med3_f32 v86, v86, s76, v237
	v_med3_f32 v87, v87, s76, v237
	v_med3_f32 v88, v88, s76, v237
	v_med3_f32 v89, v89, s76, v237
	v_cvt_pk_fp8_f32 v27, v86, v87
	v_cvt_pk_fp8_f32 v27, v88, v89 op_sel:[0,0,1]
	v_add_u32_e32 v30, 0xa0, v6
	v_ashrrev_i32_e32 v31, 31, v30
	v_lshlrev_b64 v[30:31], 10, v[30:31]
	v_lshl_add_u64 v[30:31], v[30:31], 0, v[2:3]
	global_store_dwordx2 v[30:31], v[26:27], off
	v_mul_f32_e32 v28, 0x41800000, v4
	v_pk_mul_f32 v[78:79], v[78:79], v[4:5] op_sel_hi:[1,0]
	v_pk_mul_f32 v[80:81], v[80:81], v[4:5] op_sel_hi:[1,0]
	v_pk_mul_f32 v[74:75], v[74:75], v[28:29] op_sel_hi:[1,0]
	v_pk_mul_f32 v[76:77], v[76:77], v[28:29] op_sel_hi:[1,0]
	v_pk_mul_f32 v[22:23], v[78:79], s[98:99] op_sel_hi:[1,0]
	v_pk_mul_f32 v[24:25], v[80:81], s[98:99] op_sel_hi:[1,0]
	v_exp_f32_e32 v22, v22
	v_exp_f32_e32 v23, v23
	v_exp_f32_e32 v24, v24
	v_exp_f32_e32 v25, v25
	v_pk_mul_f32 v[78:79], v[78:79], v[74:75]
	v_pk_add_f32 v[22:23], v[22:23], 1.0 op_sel_hi:[1,0]
	v_pk_add_f32 v[24:25], v[24:25], 1.0 op_sel_hi:[1,0]
	v_rcp_f32_e32 v22, v22
	v_rcp_f32_e32 v23, v23
	v_rcp_f32_e32 v24, v24
	v_rcp_f32_e32 v25, v25
	v_pk_mul_f32 v[80:81], v[80:81], v[76:77]
	v_pk_mul_f32 v[78:79], v[78:79], v[22:23]
	v_pk_mul_f32 v[80:81], v[80:81], v[24:25]
	v_med3_f32 v78, v78, s76, v237
	v_med3_f32 v79, v79, s76, v237
	v_med3_f32 v80, v80, s76, v237
	v_med3_f32 v81, v81, s76, v237
	v_cvt_pk_fp8_f32 v26, v78, v79
	v_cvt_pk_fp8_f32 v26, v80, v81 op_sel:[0,0,1]
	v_pk_mul_f32 v[70:71], v[70:71], v[4:5] op_sel_hi:[1,0]
	v_pk_mul_f32 v[72:73], v[72:73], v[4:5] op_sel_hi:[1,0]
	v_pk_mul_f32 v[66:67], v[66:67], v[28:29] op_sel_hi:[1,0]
	v_pk_mul_f32 v[68:69], v[68:69], v[28:29] op_sel_hi:[1,0]
	v_pk_mul_f32 v[22:23], v[70:71], s[98:99] op_sel_hi:[1,0]
	v_pk_mul_f32 v[24:25], v[72:73], s[98:99] op_sel_hi:[1,0]
	v_exp_f32_e32 v22, v22
	v_exp_f32_e32 v23, v23
	v_exp_f32_e32 v24, v24
	v_exp_f32_e32 v25, v25
	v_pk_mul_f32 v[70:71], v[70:71], v[66:67]
	v_pk_add_f32 v[22:23], v[22:23], 1.0 op_sel_hi:[1,0]
	v_pk_add_f32 v[24:25], v[24:25], 1.0 op_sel_hi:[1,0]
	v_rcp_f32_e32 v22, v22
	v_rcp_f32_e32 v23, v23
	v_rcp_f32_e32 v24, v24
	v_rcp_f32_e32 v25, v25
	v_pk_mul_f32 v[72:73], v[72:73], v[68:69]
	v_pk_mul_f32 v[70:71], v[70:71], v[22:23]
	v_pk_mul_f32 v[72:73], v[72:73], v[24:25]
	v_med3_f32 v70, v70, s76, v237
	v_med3_f32 v71, v71, s76, v237
	v_med3_f32 v72, v72, s76, v237
	v_med3_f32 v73, v73, s76, v237
	v_cvt_pk_fp8_f32 v27, v70, v71
	v_cvt_pk_fp8_f32 v27, v72, v73 op_sel:[0,0,1]
	v_add_u32_e32 v30, 0xb0, v6
	v_ashrrev_i32_e32 v31, 31, v30
	v_lshlrev_b64 v[30:31], 10, v[30:31]
	v_lshl_add_u64 v[30:31], v[30:31], 0, v[2:3]
	global_store_dwordx2 v[30:31], v[26:27], off
	s_andn2_b64 vcc, exec, s[26:27]
	s_mov_b64 s[26:27], -1
	s_cbranch_vccnz .LBB0_5214
	s_andn2_b64 vcc, exec, s[12:13]
	s_cbranch_vccnz .LBB0_5213
	s_barrier
	s_branch .LBB0_5213
